# v63 + P5 epilogue head: removed the vmcnt(0) drain (bias already complete; the next unit's B loads stay in flight through the epilogue instead of being waited on)
# baseline (speedup 1.0000x reference)
.LBB0_648:
	s_mov_b32 m0, s85
	ds_read_b64_tr_b16 v[198:199], v187
	ds_read_b64_tr_b16 v[180:181], v187 offset:32
	ds_read_b64_tr_b16 v[202:203], v187 offset:64
	ds_read_b64_tr_b16 v[176:177], v187 offset:96
	ds_read_b64_tr_b16 v[200:201], v188
	ds_read_b64_tr_b16 v[182:183], v188 offset:32
	ds_read_b64_tr_b16 v[204:205], v188 offset:64
	ds_read_b64_tr_b16 v[178:179], v188 offset:96
	ds_read_b128 v[206:209], v186
	ds_read_b128 v[210:213], v186 offset:2048
	ds_read_b128 v[214:217], v186 offset:4096
	buffer_load_dwordx4 v189, s[20:23], s49 offen lds
	s_mov_b32 m0, s7
	s_add_i32 s16, s65, -1
	buffer_load_dwordx4 v192, s[20:23], s49 offen lds
	s_mov_b32 m0, s6
	s_and_b32 s25, s67, 0xffff
	buffer_load_dwordx4 v191, s[20:23], s49 offen lds
	s_mov_b32 m0, s47
	s_mov_b32 s24, s66
	buffer_load_dwordx4 v190, s[20:23], s49 offen lds
	s_mov_b32 m0, s48
	s_mov_b32 s26, s18
	buffer_load_dwordx4 v193, s[20:23], s49 offen lds
	v_mbcnt_lo_u32_b32 v189, -1, 0
	v_mbcnt_hi_u32_b32 v189, -1, v189
	s_mov_b32 s27, s19
	v_ashrrev_i32_e32 v190, 2, v189
	v_add_u32_e32 v190, s78, v190
	v_add_u32_e32 v191, s81, v190
	v_min_i32_e32 v192, s16, v191
	v_add_u32_e32 v193, 64, v191
	v_add_u32_e32 v195, 0x80, v191
	v_add_u32_e32 v191, 0xc0, v191
	v_add_u32_e32 v190, s82, v190
	v_min_i32_e32 v193, s16, v193
	v_min_i32_e32 v195, s16, v195
	v_min_i32_e32 v191, s16, v191
	v_min_i32_e32 v190, s16, v190
	v_lshlrev_b32_e32 v192, 2, v192
	v_lshlrev_b32_e32 v193, 2, v193
	v_lshlrev_b32_e32 v195, 2, v195
	v_lshlrev_b32_e32 v191, 2, v191
	v_lshlrev_b32_e32 v190, 2, v190
	buffer_load_dword v192, v192, s[24:27], 0 offen
	s_nop 0
	buffer_load_dword v193, v193, s[24:27], 0 offen
	s_nop 0
	buffer_load_dword v195, v195, s[24:27], 0 offen
	s_nop 0
	buffer_load_dword v191, v191, s[24:27], 0 offen
	s_nop 0
	buffer_load_dword v190, v190, s[24:27], 0 offen
	v_lshlrev_b32_e32 v197, 4, v189
	v_and_b32_e32 v189, 32, v189
	v_and_b32_e32 v197, 48, v197
	v_bitop3_b32 v197, v197, s84, v189 bitop3:0xde
	s_and_b32 s25, s77, 0xffff
	s_mov_b32 s24, s55
	s_and_b32 s29, s80, 0xffff
	s_mov_b32 s28, s79
	s_mov_b32 s16, s55
	s_mov_b32 s36, s79
	s_mov_b32 s38, s18
	s_mov_b32 s39, s19
	s_waitcnt lgkmcnt(2)
	v_mfma_f32_16x16x32_bf16 v[172:175], v[198:201], v[206:209], v[172:175]
	s_mov_b32 s17, s25
	s_mov_b32 s37, s29
	s_waitcnt vmcnt(10)
	v_mfma_f32_16x16x32_bf16 v[168:171], v[180:183], v[206:209], v[168:171]
	v_mfma_f32_16x16x32_bf16 v[164:167], v[202:205], v[206:209], v[164:167]
	v_mfma_f32_16x16x32_bf16 v[160:163], v[176:179], v[206:209], v[160:163]
	ds_read_b128 v[206:209], v186 offset:6144
	v_cvt_pk_bf16_f32 v15, v14, v15
	v_cvt_pk_bf16_f32 v14, v12, v13
	s_waitcnt lgkmcnt(2)
	v_mfma_f32_16x16x32_bf16 v[156:159], v[198:201], v[210:213], v[156:159]
	ds_write_b64 v185, v[14:15] offset:34816
	v_mfma_f32_16x16x32_bf16 v[152:155], v[180:183], v[210:213], v[152:155]
	v_mfma_f32_16x16x32_bf16 v[148:151], v[202:205], v[210:213], v[148:151]
	v_mfma_f32_16x16x32_bf16 v[144:147], v[176:179], v[210:213], v[144:147]
	buffer_load_dwordx4 v[12:15], v184, s[16:19], 0 offen
	ds_read_b128 v[210:213], v186 offset:8192
	s_waitcnt lgkmcnt(3)
	v_mfma_f32_16x16x32_bf16 v[132:135], v[198:201], v[214:217], v[132:135]
	v_mfma_f32_16x16x32_bf16 v[124:127], v[180:183], v[214:217], v[124:127]
	v_mfma_f32_16x16x32_bf16 v[120:123], v[202:205], v[214:217], v[120:123]
	v_mfma_f32_16x16x32_bf16 v[140:143], v[176:179], v[214:217], v[140:143]
	ds_read_b128 v[214:217], v186 offset:10240
	v_cvt_pk_bf16_f32 v3, v2, v3
	v_cvt_pk_bf16_f32 v2, v0, v1
	s_waitcnt lgkmcnt(3)
	v_mfma_f32_16x16x32_bf16 v[136:139], v[198:201], v[206:209], v[136:139]
	ds_write_b64 v185, v[2:3] offset:43520
	v_mfma_f32_16x16x32_bf16 v[128:131], v[180:183], v[206:209], v[128:131]
	v_mfma_f32_16x16x32_bf16 v[116:119], v[202:205], v[206:209], v[116:119]
	v_mfma_f32_16x16x32_bf16 v[112:115], v[176:179], v[206:209], v[112:115]
	buffer_load_dwordx4 v[0:3], v184, s[16:19], s19 offen
	ds_read_b128 v[206:209], v186 offset:12288
	s_waitcnt lgkmcnt(3)
	v_mfma_f32_16x16x32_bf16 v[100:103], v[198:201], v[210:213], v[100:103]
	v_mfma_f32_16x16x32_bf16 v[92:95], v[180:183], v[210:213], v[92:95]
	v_mfma_f32_16x16x32_bf16 v[88:91], v[202:205], v[210:213], v[88:91]
	v_mfma_f32_16x16x32_bf16 v[108:111], v[176:179], v[210:213], v[108:111]
	ds_read_b128 v[210:213], v186 offset:14336
	v_cvt_pk_bf16_f32 v31, v30, v31
	v_cvt_pk_bf16_f32 v30, v28, v29
	s_waitcnt lgkmcnt(3)
	v_mfma_f32_16x16x32_bf16 v[104:107], v[198:201], v[214:217], v[104:107]
	ds_write_b64 v185, v[30:31] offset:52224
	v_mfma_f32_16x16x32_bf16 v[96:99], v[180:183], v[214:217], v[96:99]
	v_mfma_f32_16x16x32_bf16 v[84:87], v[202:205], v[214:217], v[84:87]
	v_mfma_f32_16x16x32_bf16 v[80:83], v[176:179], v[214:217], v[80:83]
	buffer_load_dwordx4 v[28:31], v184, s[16:19], s87 offen
	ds_read_b128 v[214:217], v186 offset:16384
	s_waitcnt lgkmcnt(3)
	v_mfma_f32_16x16x32_bf16 v[72:75], v[198:201], v[206:209], v[72:75]
	v_mfma_f32_16x16x32_bf16 v[64:67], v[180:183], v[206:209], v[64:67]
	v_mfma_f32_16x16x32_bf16 v[60:63], v[202:205], v[206:209], v[60:63]
	v_mfma_f32_16x16x32_bf16 v[76:79], v[176:179], v[206:209], v[76:79]
	ds_read_b128 v[206:209], v186 offset:1024
	v_cvt_pk_bf16_f32 v27, v26, v27
	v_cvt_pk_bf16_f32 v26, v24, v25
	s_waitcnt lgkmcnt(3)
	v_mfma_f32_16x16x32_bf16 v[68:71], v[198:201], v[210:213], v[68:71]
	ds_write_b64 v185, v[26:27] offset:60928
	v_mfma_f32_16x16x32_bf16 v[56:59], v[180:183], v[210:213], v[56:59]
	v_mfma_f32_16x16x32_bf16 v[52:55], v[202:205], v[210:213], v[52:55]
	v_mfma_f32_16x16x32_bf16 v[48:51], v[176:179], v[210:213], v[48:51]
	buffer_load_dwordx4 v[24:27], v184, s[16:19], s88 offen
	ds_read_b128 v[210:213], v186 offset:3072
	s_waitcnt lgkmcnt(3)
	v_mfma_f32_16x16x32_bf16 v[44:47], v[198:201], v[214:217], v[44:47]
	ds_read_b64_tr_b16 v[200:201], v188 offset:17408
	ds_read_b64_tr_b16 v[220:221], v188 offset:17440
	ds_read_b64_tr_b16 v[198:199], v187 offset:17408
	ds_read_b64_tr_b16 v[218:219], v187 offset:17440
	v_mfma_f32_16x16x32_bf16 v[40:43], v[180:183], v[214:217], v[40:43]
	ds_read_b64_tr_b16 v[180:181], v187 offset:17472
	ds_read_b64_tr_b16 v[182:183], v188 offset:17472
	v_mfma_f32_16x16x32_bf16 v[32:35], v[176:179], v[214:217], v[32:35]
	ds_read_b64_tr_b16 v[176:177], v187 offset:17504
	ds_read_b64_tr_b16 v[178:179], v188 offset:17504
	v_mfma_f32_16x16x32_bf16 v[36:39], v[202:205], v[214:217], v[36:39]
	ds_read_b128 v[202:205], v186 offset:5120
	v_cvt_pk_bf16_f32 v23, v22, v23
	v_cvt_pk_bf16_f32 v22, v20, v21
	s_waitcnt lgkmcnt(6)
	v_mfma_f32_16x16x32_bf16 v[172:175], v[198:201], v[206:209], v[172:175]
	ds_write_b64 v185, v[22:23] offset:34880
	s_waitcnt lgkmcnt(6)
	v_mfma_f32_16x16x32_bf16 v[168:171], v[218:221], v[206:209], v[168:171]
	s_waitcnt lgkmcnt(4)
	v_mfma_f32_16x16x32_bf16 v[164:167], v[180:183], v[206:209], v[164:167]
	s_waitcnt lgkmcnt(2)
	v_mfma_f32_16x16x32_bf16 v[160:163], v[176:179], v[206:209], v[160:163]
	buffer_load_dwordx4 v[20:23], v184, s[36:39], 0 offen
	ds_read_b128 v[206:209], v186 offset:7168
	v_mfma_f32_16x16x32_bf16 v[156:159], v[198:201], v[210:213], v[156:159]
	v_mfma_f32_16x16x32_bf16 v[152:155], v[218:221], v[210:213], v[152:155]
	v_mfma_f32_16x16x32_bf16 v[148:151], v[180:183], v[210:213], v[148:151]
	v_mfma_f32_16x16x32_bf16 v[144:147], v[176:179], v[210:213], v[144:147]
	ds_read_b128 v[210:213], v186 offset:9216
	v_cvt_pk_bf16_f32 v7, v6, v7
	v_cvt_pk_bf16_f32 v6, v4, v5
	s_waitcnt lgkmcnt(3)
	v_mfma_f32_16x16x32_bf16 v[132:135], v[198:201], v[202:205], v[132:135]
	ds_write_b64 v185, v[6:7] offset:43584
	v_mfma_f32_16x16x32_bf16 v[124:127], v[218:221], v[202:205], v[124:127]
	v_mfma_f32_16x16x32_bf16 v[120:123], v[180:183], v[202:205], v[120:123]
	v_mfma_f32_16x16x32_bf16 v[140:143], v[176:179], v[202:205], v[140:143]
	buffer_load_dwordx4 v[4:7], v184, s[36:39], s19 offen
	ds_read_b128 v[202:205], v186 offset:11264
	s_waitcnt lgkmcnt(3)
	v_mfma_f32_16x16x32_bf16 v[136:139], v[198:201], v[206:209], v[136:139]
	v_mfma_f32_16x16x32_bf16 v[128:131], v[218:221], v[206:209], v[128:131]
	v_mfma_f32_16x16x32_bf16 v[116:119], v[180:183], v[206:209], v[116:119]
	v_mfma_f32_16x16x32_bf16 v[112:115], v[176:179], v[206:209], v[112:115]
	ds_read_b128 v[206:209], v186 offset:13312
	v_cvt_pk_bf16_f32 v11, v10, v11
	v_cvt_pk_bf16_f32 v10, v8, v9
	s_waitcnt lgkmcnt(3)
	v_mfma_f32_16x16x32_bf16 v[100:103], v[198:201], v[210:213], v[100:103]
	ds_write_b64 v185, v[10:11] offset:52288
	v_mfma_f32_16x16x32_bf16 v[92:95], v[218:221], v[210:213], v[92:95]
	v_mfma_f32_16x16x32_bf16 v[88:91], v[180:183], v[210:213], v[88:91]
	v_mfma_f32_16x16x32_bf16 v[108:111], v[176:179], v[210:213], v[108:111]
	buffer_load_dwordx4 v[8:11], v184, s[36:39], s87 offen
	ds_read_b128 v[210:213], v186 offset:15360
	s_waitcnt lgkmcnt(3)
	v_mfma_f32_16x16x32_bf16 v[104:107], v[198:201], v[202:205], v[104:107]
	v_mfma_f32_16x16x32_bf16 v[96:99], v[218:221], v[202:205], v[96:99]
	v_mfma_f32_16x16x32_bf16 v[84:87], v[180:183], v[202:205], v[84:87]
	v_mfma_f32_16x16x32_bf16 v[80:83], v[176:179], v[202:205], v[80:83]
	ds_read_b128 v[202:205], v186 offset:17408
	v_cvt_pk_bf16_f32 v19, v18, v19
	v_cvt_pk_bf16_f32 v18, v16, v17
	s_waitcnt lgkmcnt(3)
	v_mfma_f32_16x16x32_bf16 v[72:75], v[198:201], v[206:209], v[72:75]
	ds_write_b64 v185, v[18:19] offset:60992
	v_mfma_f32_16x16x32_bf16 v[64:67], v[218:221], v[206:209], v[64:67]
	v_mfma_f32_16x16x32_bf16 v[60:63], v[180:183], v[206:209], v[60:63]
	v_mfma_f32_16x16x32_bf16 v[76:79], v[176:179], v[206:209], v[76:79]
	buffer_load_dwordx4 v[16:19], v184, s[36:39], s88 offen
	s_waitcnt lgkmcnt(2)
	v_mfma_f32_16x16x32_bf16 v[68:71], v[198:201], v[210:213], v[68:71]
	v_mfma_f32_16x16x32_bf16 v[56:59], v[218:221], v[210:213], v[56:59]
	v_mfma_f32_16x16x32_bf16 v[52:55], v[180:183], v[210:213], v[52:55]
	v_mfma_f32_16x16x32_bf16 v[48:51], v[176:179], v[210:213], v[48:51]
	s_waitcnt lgkmcnt(1)
	v_mfma_f32_16x16x32_bf16 v[44:47], v[198:201], v[202:205], v[44:47]
	v_mfma_f32_16x16x32_bf16 v[40:43], v[218:221], v[202:205], v[40:43]
	v_mfma_f32_16x16x32_bf16 v[36:39], v[180:183], v[202:205], v[36:39]
	v_mfma_f32_16x16x32_bf16 v[32:35], v[176:179], v[202:205], v[32:35]
	s_waitcnt vmcnt(8)
	v_lshlrev_b32_e32 v189, 10, v192
	v_lshlrev_b32_e32 v192, 10, v193
	v_lshlrev_b32_e32 v193, 10, v195
	v_lshlrev_b32_e32 v195, 10, v191
	v_lshlrev_b32_e32 v243, 10, v190
	v_and_or_b32 v189, v189, s83, v197
	v_and_or_b32 v192, v192, s83, v197
	v_and_or_b32 v191, v193, s83, v197
	v_and_or_b32 v190, v195, s83, v197
	v_and_or_b32 v193, v243, s83, v197
	s_mov_b32 m0, s46
	s_waitcnt lgkmcnt(0)
	s_barrier
	v_mbcnt_lo_u32_b32 v244, -1, 0
	v_mbcnt_hi_u32_b32 v244, -1, v244
	s_add_i32 s100, s54, s4
	v_ashrrev_i32_e32 v238, 1, v244
	v_and_b32_e32 v238, -8, v238
	v_add_u32_e32 v244, s100, v238
	v_ashrrev_i32_e32 v245, 31, v244
	v_lshlrev_b64 v[238:239], 2, v[244:245]
	v_lshl_add_u64 v[240:241], s[56:57], 0, v[238:239]
	v_lshl_add_u64 v[238:239], s[58:59], 0, v[238:239]
	global_load_dwordx4 v[252:255], v[240:241], off
	global_load_dwordx4 v[248:251], v[238:239], off
	global_load_dwordx4 v[244:247], v[240:241], off offset:16
	s_nop 0
	global_load_dwordx4 v[238:241], v[238:239], off offset:16
	ds_read_b64_tr_b16 v[178:179], v188 offset:34816
	ds_read_b64_tr_b16 v[176:177], v187 offset:34816
	ds_read_b64_tr_b16 v[180:181], v187 offset:34848
	ds_read_b64_tr_b16 v[198:199], v187 offset:34880
	ds_read_b64_tr_b16 v[202:203], v187 offset:34912
	ds_read_b128 v[206:209], v186 offset:36864
	ds_read_b64_tr_b16 v[182:183], v188 offset:34848
	ds_read_b64_tr_b16 v[200:201], v188 offset:34880
	ds_read_b64_tr_b16 v[204:205], v188 offset:34912
	ds_read_b128 v[210:213], v186 offset:38912
	ds_read_b128 v[214:217], v186 offset:40960
	buffer_load_dwordx4 v189, s[20:23], 0 offen lds
	s_mov_b32 m0, s86
	s_waitcnt lgkmcnt(5)
	v_mfma_f32_16x16x32_bf16 v[172:175], v[176:179], v[206:209], v[172:175]
	buffer_load_dwordx4 v192, s[20:23], 0 offen lds
	s_mov_b32 m0, s89
	s_nop 0
	buffer_load_dwordx4 v191, s[20:23], 0 offen lds
	s_mov_b32 m0, s90
	s_waitcnt lgkmcnt(4)
	v_mfma_f32_16x16x32_bf16 v[168:171], v[180:183], v[206:209], v[168:171]
	buffer_load_dwordx4 v190, s[20:23], 0 offen lds
	s_mov_b32 m0, s91
	s_nop 0
	buffer_load_dwordx4 v193, s[20:23], 0 offen lds
	s_waitcnt lgkmcnt(3)
	v_mfma_f32_16x16x32_bf16 v[164:167], v[198:201], v[206:209], v[164:167]
	s_waitcnt lgkmcnt(2)
	v_mfma_f32_16x16x32_bf16 v[160:163], v[202:205], v[206:209], v[160:163]
	ds_read_b128 v[206:209], v186 offset:43008
	s_waitcnt vmcnt(16)
	v_cvt_pk_bf16_f32 v15, v14, v15
	v_cvt_pk_bf16_f32 v14, v12, v13
	s_waitcnt lgkmcnt(2)
	v_mfma_f32_16x16x32_bf16 v[156:159], v[176:179], v[210:213], v[156:159]
	ds_write_b64 v185, v[14:15]
	v_mfma_f32_16x16x32_bf16 v[152:155], v[180:183], v[210:213], v[152:155]
	v_mfma_f32_16x16x32_bf16 v[148:151], v[198:201], v[210:213], v[148:151]
	v_mfma_f32_16x16x32_bf16 v[144:147], v[202:205], v[210:213], v[144:147]
	buffer_load_dwordx4 v[12:15], v184, s[16:19], s93 offen
	ds_read_b128 v[210:213], v186 offset:45056
	s_waitcnt lgkmcnt(3)
	v_mfma_f32_16x16x32_bf16 v[132:135], v[176:179], v[214:217], v[132:135]
	v_mfma_f32_16x16x32_bf16 v[124:127], v[180:183], v[214:217], v[124:127]
	v_mfma_f32_16x16x32_bf16 v[120:123], v[198:201], v[214:217], v[120:123]
	v_mfma_f32_16x16x32_bf16 v[140:143], v[202:205], v[214:217], v[140:143]
	ds_read_b128 v[214:217], v186 offset:47104
	s_waitcnt vmcnt(16)
	v_cvt_pk_bf16_f32 v3, v2, v3
	v_cvt_pk_bf16_f32 v2, v0, v1
	s_waitcnt lgkmcnt(3)
	v_mfma_f32_16x16x32_bf16 v[136:139], v[176:179], v[206:209], v[136:139]
	ds_write_b64 v185, v[2:3] offset:8704
	v_mfma_f32_16x16x32_bf16 v[128:131], v[180:183], v[206:209], v[128:131]
	v_mfma_f32_16x16x32_bf16 v[116:119], v[198:201], v[206:209], v[116:119]
	v_mfma_f32_16x16x32_bf16 v[112:115], v[202:205], v[206:209], v[112:115]
	buffer_load_dwordx4 v[0:3], v184, s[16:19], s94 offen
	ds_read_b128 v[206:209], v186 offset:49152
	s_waitcnt lgkmcnt(3)
	v_mfma_f32_16x16x32_bf16 v[100:103], v[176:179], v[210:213], v[100:103]
	v_mfma_f32_16x16x32_bf16 v[92:95], v[180:183], v[210:213], v[92:95]
	v_mfma_f32_16x16x32_bf16 v[88:91], v[198:201], v[210:213], v[88:91]
	v_mfma_f32_16x16x32_bf16 v[108:111], v[202:205], v[210:213], v[108:111]
	ds_read_b128 v[210:213], v186 offset:51200
	s_waitcnt vmcnt(16)
	v_cvt_pk_bf16_f32 v31, v30, v31
	v_cvt_pk_bf16_f32 v30, v28, v29
	s_waitcnt lgkmcnt(3)
	v_mfma_f32_16x16x32_bf16 v[104:107], v[176:179], v[214:217], v[104:107]
	ds_write_b64 v185, v[30:31] offset:17408
	v_mfma_f32_16x16x32_bf16 v[96:99], v[180:183], v[214:217], v[96:99]
	v_mfma_f32_16x16x32_bf16 v[84:87], v[198:201], v[214:217], v[84:87]
	v_mfma_f32_16x16x32_bf16 v[80:83], v[202:205], v[214:217], v[80:83]
	buffer_load_dwordx4 v[28:31], v184, s[16:19], s95 offen
	ds_read_b128 v[214:217], v186 offset:53248
	s_waitcnt lgkmcnt(3)
	v_mfma_f32_16x16x32_bf16 v[72:75], v[176:179], v[206:209], v[72:75]
	v_mfma_f32_16x16x32_bf16 v[64:67], v[180:183], v[206:209], v[64:67]
	v_mfma_f32_16x16x32_bf16 v[60:63], v[198:201], v[206:209], v[60:63]
	v_mfma_f32_16x16x32_bf16 v[76:79], v[202:205], v[206:209], v[76:79]
	ds_read_b128 v[206:209], v186 offset:37888
	s_waitcnt vmcnt(16)
	v_cvt_pk_bf16_f32 v27, v26, v27
	v_cvt_pk_bf16_f32 v26, v24, v25
	s_waitcnt lgkmcnt(3)
	v_mfma_f32_16x16x32_bf16 v[68:71], v[176:179], v[210:213], v[68:71]
	ds_write_b64 v185, v[26:27] offset:26112
	v_mfma_f32_16x16x32_bf16 v[56:59], v[180:183], v[210:213], v[56:59]
	v_mfma_f32_16x16x32_bf16 v[52:55], v[198:201], v[210:213], v[52:55]
	v_mfma_f32_16x16x32_bf16 v[48:51], v[202:205], v[210:213], v[48:51]
	buffer_load_dwordx4 v[24:27], v184, s[16:19], s96 offen
	ds_read_b128 v[210:213], v186 offset:39936
	s_waitcnt lgkmcnt(3)
	v_mfma_f32_16x16x32_bf16 v[44:47], v[176:179], v[214:217], v[44:47]
	ds_read_b64_tr_b16 v[178:179], v188 offset:52224
	ds_read_b64_tr_b16 v[220:221], v188 offset:52256
	ds_read_b64_tr_b16 v[176:177], v187 offset:52224
	ds_read_b64_tr_b16 v[218:219], v187 offset:52256
	v_mfma_f32_16x16x32_bf16 v[40:43], v[180:183], v[214:217], v[40:43]
	v_mfma_f32_16x16x32_bf16 v[180:183], v[198:201], v[214:217], v[36:39]
	ds_read_b64_tr_b16 v[198:199], v187 offset:52288
	ds_read_b64_tr_b16 v[200:201], v188 offset:52288
	v_mfma_f32_16x16x32_bf16 v[32:35], v[202:205], v[214:217], v[32:35]
	ds_read_b64_tr_b16 v[202:203], v187 offset:52320
	ds_read_b64_tr_b16 v[204:205], v188 offset:52320
	ds_read_b128 v[36:39], v186 offset:41984
	s_waitcnt vmcnt(16)
	v_cvt_pk_bf16_f32 v23, v22, v23
	v_cvt_pk_bf16_f32 v22, v20, v21
	s_waitcnt lgkmcnt(6)
	v_mfma_f32_16x16x32_bf16 v[214:217], v[176:179], v[206:209], v[172:175]
	ds_write_b64 v185, v[22:23] offset:64
	s_waitcnt lgkmcnt(6)
	v_mfma_f32_16x16x32_bf16 v[222:225], v[218:221], v[206:209], v[168:171]
	s_waitcnt lgkmcnt(4)
	v_mfma_f32_16x16x32_bf16 v[226:229], v[198:201], v[206:209], v[164:167]
	s_waitcnt lgkmcnt(2)
	v_mfma_f32_16x16x32_bf16 v[206:209], v[202:205], v[206:209], v[160:163]
	buffer_load_dwordx4 v[20:23], v184, s[36:39], s93 offen
	ds_read_b128 v[230:233], v186 offset:44032
	v_mfma_f32_16x16x32_bf16 v[172:175], v[176:179], v[210:213], v[156:159]
	v_mfma_f32_16x16x32_bf16 v[164:167], v[218:221], v[210:213], v[152:155]
	v_mfma_f32_16x16x32_bf16 v[168:171], v[198:201], v[210:213], v[148:151]
	v_mfma_f32_16x16x32_bf16 v[160:163], v[202:205], v[210:213], v[144:147]
	ds_read_b128 v[210:213], v186 offset:46080
	s_waitcnt vmcnt(16)
	v_cvt_pk_bf16_f32 v7, v6, v7
	v_cvt_pk_bf16_f32 v6, v4, v5
	s_waitcnt lgkmcnt(3)
	v_mfma_f32_16x16x32_bf16 v[156:159], v[176:179], v[36:39], v[132:135]
	ds_write_b64 v185, v[6:7] offset:8768
	v_mfma_f32_16x16x32_bf16 v[144:147], v[218:221], v[36:39], v[124:127]
	v_mfma_f32_16x16x32_bf16 v[152:155], v[198:201], v[36:39], v[120:123]
	v_mfma_f32_16x16x32_bf16 v[148:151], v[202:205], v[36:39], v[140:143]
	buffer_load_dwordx4 v[4:7], v184, s[36:39], s94 offen
	ds_read_b128 v[36:39], v186 offset:48128
	s_waitcnt lgkmcnt(3)
	v_mfma_f32_16x16x32_bf16 v[140:143], v[176:179], v[230:233], v[136:139]
	v_mfma_f32_16x16x32_bf16 v[132:135], v[218:221], v[230:233], v[128:131]
	v_mfma_f32_16x16x32_bf16 v[136:139], v[198:201], v[230:233], v[116:119]
	v_mfma_f32_16x16x32_bf16 v[128:131], v[202:205], v[230:233], v[112:115]
	ds_read_b128 v[230:233], v186 offset:50176
	s_waitcnt vmcnt(16)
	v_cvt_pk_bf16_f32 v11, v10, v11
	v_cvt_pk_bf16_f32 v10, v8, v9
	s_waitcnt lgkmcnt(3)
	v_mfma_f32_16x16x32_bf16 v[124:127], v[176:179], v[210:213], v[100:103]
	ds_write_b64 v185, v[10:11] offset:17472
	v_mfma_f32_16x16x32_bf16 v[112:115], v[218:221], v[210:213], v[92:95]
	v_mfma_f32_16x16x32_bf16 v[120:123], v[198:201], v[210:213], v[88:91]
	v_mfma_f32_16x16x32_bf16 v[116:119], v[202:205], v[210:213], v[108:111]
	buffer_load_dwordx4 v[8:11], v184, s[36:39], s95 offen
	ds_read_b128 v[210:213], v186 offset:52224
	s_waitcnt lgkmcnt(3)
	v_mfma_f32_16x16x32_bf16 v[108:111], v[176:179], v[36:39], v[104:107]
	v_mfma_f32_16x16x32_bf16 v[100:103], v[218:221], v[36:39], v[96:99]
	v_mfma_f32_16x16x32_bf16 v[104:107], v[198:201], v[36:39], v[84:87]
	v_mfma_f32_16x16x32_bf16 v[96:99], v[202:205], v[36:39], v[80:83]
	ds_read_b128 v[234:237], v186 offset:54272
	s_waitcnt vmcnt(16)
	v_cvt_pk_bf16_f32 v19, v18, v19
	v_cvt_pk_bf16_f32 v18, v16, v17
	s_waitcnt lgkmcnt(3)
	v_mfma_f32_16x16x32_bf16 v[92:95], v[176:179], v[230:233], v[72:75]
	ds_write_b64 v185, v[18:19] offset:26176
	v_mfma_f32_16x16x32_bf16 v[80:83], v[218:221], v[230:233], v[64:67]
	v_mfma_f32_16x16x32_bf16 v[88:91], v[198:201], v[230:233], v[60:63]
	v_mfma_f32_16x16x32_bf16 v[84:87], v[202:205], v[230:233], v[76:79]
	buffer_load_dwordx4 v[16:19], v184, s[36:39], s96 offen
	s_waitcnt lgkmcnt(2)
	v_mfma_f32_16x16x32_bf16 v[76:79], v[176:179], v[210:213], v[68:71]
	v_mfma_f32_16x16x32_bf16 v[68:71], v[218:221], v[210:213], v[56:59]
	v_mfma_f32_16x16x32_bf16 v[72:75], v[198:201], v[210:213], v[52:55]
	v_mfma_f32_16x16x32_bf16 v[64:67], v[202:205], v[210:213], v[48:51]
	s_waitcnt lgkmcnt(1)
	v_mfma_f32_16x16x32_bf16 v[52:55], v[176:179], v[234:237], v[44:47]
	v_mfma_f32_16x16x32_bf16 v[36:39], v[218:221], v[234:237], v[40:43]
	v_mfma_f32_16x16x32_bf16 v[48:51], v[198:201], v[234:237], v[180:183]
	v_mfma_f32_16x16x32_bf16 v[32:35], v[202:205], v[234:237], v[32:35]
	s_waitcnt vmcnt(8)
	s_waitcnt lgkmcnt(0)
	s_barrier
	v_mbcnt_lo_u32_b32 v178, -1, 0
	v_mbcnt_hi_u32_b32 v178, -1, v178
	s_add_i32 s16, s54, s4
	v_ashrrev_i32_e32 v40, 1, v178
	v_and_b32_e32 v40, -8, v40
	v_add_u32_e32 v176, s16, v40
	v_ashrrev_i32_e32 v177, 31, v176
	v_lshlrev_b64 v[40:41], 2, v[176:177]
	v_lshl_add_u64 v[42:43], s[56:57], 0, v[40:41]
	v_lshl_add_u64 v[40:41], s[58:59], 0, v[40:41]
	s_nop 0
	s_mul_i32 s16, s72, 0x90
	v_and_or_b32 v178, v178, 15, s16
	v_add_u32_e32 v180, s68, v178
	v_ashrrev_i32_e32 v181, 31, v180
	v_lshlrev_b64 v[180:181], 12, v[180:181]
	v_lshl_add_u64 v[198:199], s[50:51], 0, v[180:181]
	v_lshlrev_b64 v[176:177], 1, v[176:177]
	v_lshl_add_u64 v[198:199], v[198:199], 0, v[176:177]
	s_add_i32 s16, s68, 0x50
	s_and_b64 vcc, exec, s[30:31]
	s_mov_b32 s54, s42
	s_mov_b64 s[58:59], s[62:63]
	s_mov_b64 s[56:57], s[60:61]
	s_mov_b64 s[30:31], s[18:19]
	s_mov_b64 s[26:27], s[18:19]
	v_add_f32_e32 v179, v214, v252
	v_add_f32_e32 v181, v226, v248
	v_add_f32_e32 v183, v215, v253
	v_add_f32_e32 v197, v216, v254
	v_add_f32_e32 v201, v228, v250
	v_add_f32_e32 v203, v217, v255
	v_add_f32_e32 v195, v227, v249
	v_add_f32_e32 v204, v229, v251
	v_add_f32_e32 v205, v222, v244
	v_add_f32_e32 v210, v223, v245
	v_add_f32_e32 v211, v224, v246
	v_add_f32_e32 v212, v208, v240
	v_add_f32_e32 v213, v225, v247
	v_min_f32_e32 v180, 0x40e00000, v179
	v_med3_f32 v182, v181, s53, v194
	v_min_f32_e32 v181, 0x40e00000, v183
	v_min_f32_e32 v200, 0x40e00000, v197
	v_med3_f32 v202, v201, s53, v194
	v_min_f32_e32 v201, 0x40e00000, v203
	v_add_f32_e32 v214, v209, v241
	v_med3_f32 v183, v195, s53, v194
	v_med3_f32 v203, v204, s53, v194
	v_min_f32_e32 v204, 0x40e00000, v205
	v_min_f32_e32 v205, 0x40e00000, v210
	v_min_f32_e32 v208, 0x40e00000, v211
	v_med3_f32 v210, v212, s53, v194
	v_min_f32_e32 v209, 0x40e00000, v213
	v_mul_f32_e32 v179, 0x3fd9db23, v180
	v_mul_f32_e32 v195, 0x3fd9db23, v181
	v_mul_f32_e32 v197, 0x3fd9db23, v200
	v_mul_f32_e32 v212, 0x3fd9db23, v201
	v_med3_f32 v211, v214, s53, v194
	v_pk_add_f32 v[182:183], v[182:183], 1.0 op_sel_hi:[1,0]
	v_pk_add_f32 v[202:203], v[202:203], 1.0 op_sel_hi:[1,0]
	v_mul_f32_e32 v213, 0x3fd9db23, v204
	v_mul_f32_e32 v214, 0x3fd9db23, v205
	v_mul_f32_e32 v215, 0x3fd9db23, v208
	v_mul_f32_e32 v216, 0x3fd9db23, v209
	v_mul_f32_e32 v179, 0xbfb8aa3b, v179
	v_mul_f32_e32 v195, 0xbfb8aa3b, v195
	v_mul_f32_e32 v197, 0xbfb8aa3b, v197
	v_mul_f32_e32 v212, 0xbfb8aa3b, v212
	v_pk_mul_f32 v[200:201], v[200:201], v[202:203]
	v_pk_mul_f32 v[180:181], v[180:181], v[182:183]
	v_mul_f32_e32 v182, 0xbfb8aa3b, v213
	v_mul_f32_e32 v183, 0xbfb8aa3b, v214
	v_mul_f32_e32 v202, 0xbfb8aa3b, v215
	v_mul_f32_e32 v203, 0xbfb8aa3b, v216
	v_exp_f32_e32 v179, v179
	v_exp_f32_e32 v195, v195
	v_exp_f32_e32 v197, v197
	v_exp_f32_e32 v212, v212
	v_exp_f32_e32 v182, v182
	v_exp_f32_e32 v183, v183
	v_exp_f32_e32 v202, v202
	v_exp_f32_e32 v203, v203
	v_add_f32_e32 v179, 1.0, v179
	v_add_f32_e32 v195, 1.0, v195
	v_add_f32_e32 v197, 1.0, v197
	v_add_f32_e32 v212, 1.0, v212
	v_add_f32_e32 v213, 1.0, v182
	v_add_f32_e32 v214, 1.0, v183
	v_add_f32_e32 v215, 1.0, v202
	v_add_f32_e32 v216, 1.0, v203
	v_rcp_f32_e32 v182, v179
	v_rcp_f32_e32 v183, v195
	v_rcp_f32_e32 v202, v197
	v_rcp_f32_e32 v203, v212
	v_add_f32_e32 v206, v206, v238
	v_add_f32_e32 v207, v207, v239
	v_rcp_f32_e32 v212, v213
	v_rcp_f32_e32 v213, v214
	v_rcp_f32_e32 v214, v215
	v_rcp_f32_e32 v215, v216
	v_med3_f32 v206, v206, s53, v194
	v_med3_f32 v207, v207, s53, v194
	v_pk_mul_f32 v[182:183], v[180:181], v[182:183]
	v_pk_mul_f32 v[180:181], v[200:201], v[202:203]
	v_pk_add_f32 v[206:207], v[206:207], 1.0 op_sel_hi:[1,0]
	v_cvt_pk_bf16_f32 v181, v180, v181
	v_cvt_pk_bf16_f32 v180, v182, v183
	v_pk_add_f32 v[182:183], v[210:211], 1.0 op_sel_hi:[1,0]
	v_pk_mul_f32 v[200:201], v[204:205], v[206:207]
	v_pk_mul_f32 v[182:183], v[208:209], v[182:183]
	v_add_f32_e32 v172, v172, v252
	v_pk_mul_f32 v[200:201], v[200:201], v[212:213]
	v_pk_mul_f32 v[182:183], v[182:183], v[214:215]
	v_min_f32_e32 v172, 0x40e00000, v172
	v_add_f32_e32 v173, v173, v253
	v_cvt_pk_bf16_f32 v183, v182, v183
	v_cvt_pk_bf16_f32 v182, v200, v201
	v_mul_f32_e32 v179, 0x3fd9db23, v172
	v_min_f32_e32 v173, 0x40e00000, v173
	global_store_dwordx4 v[198:199], v[180:183], off
	v_mul_f32_e32 v179, 0xbfb8aa3b, v179
	v_exp_f32_e32 v179, v179
	v_mul_f32_e32 v182, 0x3fd9db23, v173
	v_mul_f32_e32 v182, 0xbfb8aa3b, v182
	v_exp_f32_e32 v183, v182
	v_add_f32_e32 v174, v174, v254
	v_add_f32_e32 v179, 1.0, v179
	v_min_f32_e32 v174, 0x40e00000, v174
	v_rcp_f32_e32 v182, v179
	v_add_f32_e32 v179, 1.0, v183
	v_mul_f32_e32 v183, 0x3fd9db23, v174
	v_mul_f32_e32 v183, 0xbfb8aa3b, v183
	v_exp_f32_e32 v195, v183
	v_add_f32_e32 v175, v175, v255
	v_min_f32_e32 v175, 0x40e00000, v175
	v_rcp_f32_e32 v183, v179
	v_add_f32_e32 v179, 1.0, v195
	v_mul_f32_e32 v195, 0x3fd9db23, v175
	v_mul_f32_e32 v195, 0xbfb8aa3b, v195
	v_exp_f32_e32 v195, v195
	v_rcp_f32_e32 v198, v179
	v_add_f32_e32 v168, v168, v248
	v_add_f32_e32 v169, v169, v249
	v_add_f32_e32 v179, 1.0, v195
	v_add_f32_e32 v170, v170, v250
	v_add_f32_e32 v171, v171, v251
	v_rcp_f32_e32 v199, v179
	v_med3_f32 v168, v168, s53, v194
	v_med3_f32 v169, v169, s53, v194
	v_med3_f32 v170, v170, s53, v194
	v_med3_f32 v171, v171, s53, v194
	v_pk_add_f32 v[168:169], v[168:169], 1.0 op_sel_hi:[1,0]
	v_pk_add_f32 v[170:171], v[170:171], 1.0 op_sel_hi:[1,0]
	v_pk_mul_f32 v[168:169], v[172:173], v[168:169]
	v_pk_mul_f32 v[170:171], v[174:175], v[170:171]
	v_add_f32_e32 v164, v164, v244
	v_pk_mul_f32 v[172:173], v[168:169], v[182:183]
	v_pk_mul_f32 v[168:169], v[170:171], v[198:199]
	v_min_f32_e32 v164, 0x40e00000, v164
	v_cvt_pk_bf16_f32 v169, v168, v169
	v_mul_f32_e32 v168, 0x3fd9db23, v164
	v_add_f32_e32 v166, v166, v246
	v_add_f32_e32 v167, v167, v247
	v_mul_f32_e32 v168, 0xbfb8aa3b, v168
	v_add_f32_e32 v165, v165, v245
	v_min_f32_e32 v166, 0x40e00000, v166
	v_min_f32_e32 v167, 0x40e00000, v167
	v_exp_f32_e32 v170, v168
	v_cvt_pk_bf16_f32 v168, v172, v173
	v_min_f32_e32 v165, 0x40e00000, v165
	v_mul_f32_e32 v172, 0x3fd9db23, v166
	v_mul_f32_e32 v173, 0x3fd9db23, v167
	v_mul_f32_e32 v171, 0x3fd9db23, v165
	v_mul_f32_e32 v172, 0xbfb8aa3b, v172
	v_mul_f32_e32 v173, 0xbfb8aa3b, v173
	v_mul_f32_e32 v171, 0xbfb8aa3b, v171
	v_exp_f32_e32 v172, v172
	v_exp_f32_e32 v173, v173
	v_exp_f32_e32 v171, v171
	v_add_f32_e32 v170, 1.0, v170
	v_add_f32_e32 v172, 1.0, v172
	v_add_f32_e32 v173, 1.0, v173
	v_add_f32_e32 v171, 1.0, v171
	v_add_f32_e32 v162, v162, v240
	v_rcp_f32_e32 v172, v172
	v_add_f32_e32 v163, v163, v241
	v_rcp_f32_e32 v173, v173
	v_add_f32_e32 v160, v160, v238
	v_rcp_f32_e32 v170, v170
	v_add_f32_e32 v161, v161, v239
	v_rcp_f32_e32 v171, v171
	v_med3_f32 v162, v162, s53, v194
	v_med3_f32 v163, v163, s53, v194
	v_med3_f32 v160, v160, s53, v194
	v_med3_f32 v161, v161, s53, v194
	v_pk_add_f32 v[162:163], v[162:163], 1.0 op_sel_hi:[1,0]
	v_pk_add_f32 v[160:161], v[160:161], 1.0 op_sel_hi:[1,0]
	v_pk_mul_f32 v[162:163], v[166:167], v[162:163]
	v_add_f32_e32 v156, v156, v252
	v_add_f32_e32 v157, v157, v253
	v_add_f32_e32 v158, v158, v254
	v_add_f32_e32 v159, v159, v255
	v_pk_mul_f32 v[160:161], v[164:165], v[160:161]
	v_pk_mul_f32 v[162:163], v[162:163], v[172:173]
	v_min_f32_e32 v156, 0x40e00000, v156
	v_min_f32_e32 v157, 0x40e00000, v157
	v_min_f32_e32 v158, 0x40e00000, v158
	v_min_f32_e32 v159, 0x40e00000, v159
	v_pk_mul_f32 v[160:161], v[160:161], v[170:171]
	v_cvt_pk_bf16_f32 v171, v162, v163
	v_mul_f32_e32 v162, 0x3fd9db23, v156
	v_mul_f32_e32 v163, 0x3fd9db23, v157
	v_mul_f32_e32 v164, 0x3fd9db23, v158
	v_mul_f32_e32 v165, 0x3fd9db23, v159
	v_mul_f32_e32 v162, 0xbfb8aa3b, v162
	v_mul_f32_e32 v163, 0xbfb8aa3b, v163
	v_mul_f32_e32 v164, 0xbfb8aa3b, v164
	v_mul_f32_e32 v165, 0xbfb8aa3b, v165
	v_exp_f32_e32 v162, v162
	v_exp_f32_e32 v163, v163
	v_exp_f32_e32 v164, v164
	v_exp_f32_e32 v165, v165
	v_add_f32_e32 v162, 1.0, v162
	v_add_f32_e32 v163, 1.0, v163
	v_add_f32_e32 v164, 1.0, v164
	v_add_f32_e32 v165, 1.0, v165
	v_add_f32_e32 v152, v152, v248
	v_rcp_f32_e32 v162, v162
	v_add_f32_e32 v153, v153, v249
	v_rcp_f32_e32 v163, v163
	v_add_f32_e32 v154, v154, v250
	v_rcp_f32_e32 v164, v164
	v_add_f32_e32 v155, v155, v251
	v_rcp_f32_e32 v165, v165
	v_med3_f32 v152, v152, s53, v194
	v_med3_f32 v153, v153, s53, v194
	v_med3_f32 v154, v154, s53, v194
	v_med3_f32 v155, v155, s53, v194
	v_pk_add_f32 v[152:153], v[152:153], 1.0 op_sel_hi:[1,0]
	v_pk_add_f32 v[154:155], v[154:155], 1.0 op_sel_hi:[1,0]
	v_pk_mul_f32 v[152:153], v[156:157], v[152:153]
	v_pk_mul_f32 v[154:155], v[158:159], v[154:155]
	v_add_f32_e32 v144, v144, v244
	v_pk_mul_f32 v[156:157], v[152:153], v[162:163]
	v_pk_mul_f32 v[152:153], v[154:155], v[164:165]
	v_min_f32_e32 v144, 0x40e00000, v144
	v_cvt_pk_bf16_f32 v153, v152, v153
	v_mul_f32_e32 v152, 0x3fd9db23, v144
	v_add_f32_e32 v146, v146, v246
	v_add_f32_e32 v147, v147, v247
	v_mul_f32_e32 v152, 0xbfb8aa3b, v152
	v_add_f32_e32 v145, v145, v245
	v_min_f32_e32 v146, 0x40e00000, v146
	v_min_f32_e32 v147, 0x40e00000, v147
	v_exp_f32_e32 v154, v152
	v_cvt_pk_bf16_f32 v152, v156, v157
	v_min_f32_e32 v145, 0x40e00000, v145
	v_mul_f32_e32 v156, 0x3fd9db23, v146
	v_mul_f32_e32 v157, 0x3fd9db23, v147
	v_mul_f32_e32 v155, 0x3fd9db23, v145
	v_mul_f32_e32 v156, 0xbfb8aa3b, v156
	v_mul_f32_e32 v157, 0xbfb8aa3b, v157
	v_mul_f32_e32 v155, 0xbfb8aa3b, v155
	v_exp_f32_e32 v156, v156
	v_exp_f32_e32 v157, v157
	v_exp_f32_e32 v155, v155
	v_add_f32_e32 v154, 1.0, v154
	v_add_f32_e32 v156, 1.0, v156
	v_add_f32_e32 v157, 1.0, v157
	v_add_f32_e32 v155, 1.0, v155
	v_add_f32_e32 v150, v150, v240
	v_rcp_f32_e32 v156, v156
	v_add_f32_e32 v151, v151, v241
	v_rcp_f32_e32 v157, v157
	v_add_f32_e32 v148, v148, v238
	v_rcp_f32_e32 v154, v154
	v_add_f32_e32 v149, v149, v239
	v_rcp_f32_e32 v155, v155
	v_med3_f32 v150, v150, s53, v194
	v_med3_f32 v151, v151, s53, v194
	v_med3_f32 v148, v148, s53, v194
	v_med3_f32 v149, v149, s53, v194
	v_pk_add_f32 v[150:151], v[150:151], 1.0 op_sel_hi:[1,0]
	v_pk_add_f32 v[148:149], v[148:149], 1.0 op_sel_hi:[1,0]
	v_pk_mul_f32 v[146:147], v[146:147], v[150:151]
	v_add_f32_e32 v140, v140, v252
	v_add_f32_e32 v141, v141, v253
	v_add_f32_e32 v142, v142, v254
	v_add_f32_e32 v143, v143, v255
	v_pk_mul_f32 v[144:145], v[144:145], v[148:149]
	v_pk_mul_f32 v[146:147], v[146:147], v[156:157]
	v_min_f32_e32 v140, 0x40e00000, v140
	v_min_f32_e32 v141, 0x40e00000, v141
	v_min_f32_e32 v142, 0x40e00000, v142
	v_min_f32_e32 v143, 0x40e00000, v143
	v_pk_mul_f32 v[144:145], v[144:145], v[154:155]
	v_cvt_pk_bf16_f32 v155, v146, v147
	v_mul_f32_e32 v146, 0x3fd9db23, v140
	v_mul_f32_e32 v147, 0x3fd9db23, v141
	v_mul_f32_e32 v148, 0x3fd9db23, v142
	v_mul_f32_e32 v149, 0x3fd9db23, v143
	v_mul_f32_e32 v146, 0xbfb8aa3b, v146
	v_mul_f32_e32 v147, 0xbfb8aa3b, v147
	v_mul_f32_e32 v148, 0xbfb8aa3b, v148
	v_mul_f32_e32 v149, 0xbfb8aa3b, v149
	v_exp_f32_e32 v146, v146
	v_exp_f32_e32 v147, v147
	v_exp_f32_e32 v148, v148
	v_exp_f32_e32 v149, v149
	v_add_f32_e32 v146, 1.0, v146
	v_add_f32_e32 v147, 1.0, v147
	v_add_f32_e32 v148, 1.0, v148
	v_add_f32_e32 v149, 1.0, v149
	v_add_f32_e32 v136, v136, v248
	v_rcp_f32_e32 v146, v146
	v_add_f32_e32 v137, v137, v249
	v_rcp_f32_e32 v147, v147
	v_add_f32_e32 v138, v138, v250
	v_rcp_f32_e32 v148, v148
	v_add_f32_e32 v139, v139, v251
	v_rcp_f32_e32 v149, v149
	v_med3_f32 v136, v136, s53, v194
	v_med3_f32 v137, v137, s53, v194
	v_med3_f32 v138, v138, s53, v194
	v_med3_f32 v139, v139, s53, v194
	v_pk_add_f32 v[136:137], v[136:137], 1.0 op_sel_hi:[1,0]
	v_pk_add_f32 v[138:139], v[138:139], 1.0 op_sel_hi:[1,0]
	v_pk_mul_f32 v[136:137], v[140:141], v[136:137]
	v_pk_mul_f32 v[138:139], v[142:143], v[138:139]
	v_add_f32_e32 v132, v132, v244
	v_pk_mul_f32 v[140:141], v[136:137], v[146:147]
	v_pk_mul_f32 v[136:137], v[138:139], v[148:149]
	v_min_f32_e32 v132, 0x40e00000, v132
	v_cvt_pk_bf16_f32 v137, v136, v137
	v_mul_f32_e32 v136, 0x3fd9db23, v132
	v_add_f32_e32 v134, v134, v246
	v_add_f32_e32 v135, v135, v247
	v_mul_f32_e32 v136, 0xbfb8aa3b, v136
	v_add_f32_e32 v133, v133, v245
	v_min_f32_e32 v134, 0x40e00000, v134
	v_min_f32_e32 v135, 0x40e00000, v135
	v_exp_f32_e32 v138, v136
	v_cvt_pk_bf16_f32 v136, v140, v141
	v_min_f32_e32 v133, 0x40e00000, v133
	v_mul_f32_e32 v140, 0x3fd9db23, v134
	v_mul_f32_e32 v141, 0x3fd9db23, v135
	v_mul_f32_e32 v139, 0x3fd9db23, v133
	v_mul_f32_e32 v140, 0xbfb8aa3b, v140
	v_mul_f32_e32 v141, 0xbfb8aa3b, v141
	v_mul_f32_e32 v139, 0xbfb8aa3b, v139
	v_exp_f32_e32 v140, v140
	v_exp_f32_e32 v141, v141
	v_exp_f32_e32 v139, v139
	v_add_f32_e32 v138, 1.0, v138
	v_add_f32_e32 v140, 1.0, v140
	v_add_f32_e32 v141, 1.0, v141
	v_add_f32_e32 v139, 1.0, v139
	v_add_f32_e32 v130, v130, v240
	v_rcp_f32_e32 v140, v140
	v_add_f32_e32 v131, v131, v241
	v_rcp_f32_e32 v141, v141
	v_add_f32_e32 v128, v128, v238
	v_rcp_f32_e32 v138, v138
	v_add_f32_e32 v129, v129, v239
	v_rcp_f32_e32 v139, v139
	v_med3_f32 v130, v130, s53, v194
	v_med3_f32 v131, v131, s53, v194
	v_med3_f32 v128, v128, s53, v194
	v_med3_f32 v129, v129, s53, v194
	v_pk_add_f32 v[130:131], v[130:131], 1.0 op_sel_hi:[1,0]
	v_pk_add_f32 v[128:129], v[128:129], 1.0 op_sel_hi:[1,0]
	v_pk_mul_f32 v[130:131], v[134:135], v[130:131]
	v_add_f32_e32 v124, v124, v252
	v_add_f32_e32 v125, v125, v253
	v_add_f32_e32 v126, v126, v254
	v_add_f32_e32 v127, v127, v255
	v_pk_mul_f32 v[128:129], v[132:133], v[128:129]
	v_pk_mul_f32 v[130:131], v[130:131], v[140:141]
	v_min_f32_e32 v124, 0x40e00000, v124
	v_min_f32_e32 v125, 0x40e00000, v125
	v_min_f32_e32 v126, 0x40e00000, v126
	v_min_f32_e32 v127, 0x40e00000, v127
	v_pk_mul_f32 v[128:129], v[128:129], v[138:139]
	v_cvt_pk_bf16_f32 v139, v130, v131
	v_mul_f32_e32 v130, 0x3fd9db23, v124
	v_mul_f32_e32 v131, 0x3fd9db23, v125
	v_mul_f32_e32 v132, 0x3fd9db23, v126
	v_mul_f32_e32 v133, 0x3fd9db23, v127
	v_mul_f32_e32 v130, 0xbfb8aa3b, v130
	v_mul_f32_e32 v131, 0xbfb8aa3b, v131
	v_mul_f32_e32 v132, 0xbfb8aa3b, v132
	v_mul_f32_e32 v133, 0xbfb8aa3b, v133
	v_exp_f32_e32 v130, v130
	v_exp_f32_e32 v131, v131
	v_exp_f32_e32 v132, v132
	v_exp_f32_e32 v133, v133
	v_add_f32_e32 v130, 1.0, v130
	v_add_f32_e32 v131, 1.0, v131
	v_add_f32_e32 v132, 1.0, v132
	v_add_f32_e32 v133, 1.0, v133
	v_add_f32_e32 v120, v120, v248
	v_rcp_f32_e32 v130, v130
	v_add_f32_e32 v121, v121, v249
	v_rcp_f32_e32 v131, v131
	v_add_f32_e32 v122, v122, v250
	v_rcp_f32_e32 v132, v132
	v_add_f32_e32 v123, v123, v251
	v_rcp_f32_e32 v133, v133
	v_med3_f32 v120, v120, s53, v194
	v_med3_f32 v121, v121, s53, v194
	v_med3_f32 v122, v122, s53, v194
	v_med3_f32 v123, v123, s53, v194
	v_pk_add_f32 v[120:121], v[120:121], 1.0 op_sel_hi:[1,0]
	v_pk_add_f32 v[122:123], v[122:123], 1.0 op_sel_hi:[1,0]
	v_pk_mul_f32 v[120:121], v[124:125], v[120:121]
	v_pk_mul_f32 v[122:123], v[126:127], v[122:123]
	v_add_f32_e32 v112, v112, v244
	v_pk_mul_f32 v[124:125], v[120:121], v[130:131]
	v_pk_mul_f32 v[120:121], v[122:123], v[132:133]
	v_min_f32_e32 v112, 0x40e00000, v112
	v_cvt_pk_bf16_f32 v121, v120, v121
	v_mul_f32_e32 v120, 0x3fd9db23, v112
	v_add_f32_e32 v114, v114, v246
	v_add_f32_e32 v115, v115, v247
	v_mul_f32_e32 v120, 0xbfb8aa3b, v120
	v_add_f32_e32 v113, v113, v245
	v_min_f32_e32 v114, 0x40e00000, v114
	v_min_f32_e32 v115, 0x40e00000, v115
	v_exp_f32_e32 v122, v120
	v_cvt_pk_bf16_f32 v120, v124, v125
	v_min_f32_e32 v113, 0x40e00000, v113
	v_mul_f32_e32 v124, 0x3fd9db23, v114
	v_mul_f32_e32 v125, 0x3fd9db23, v115
	v_mul_f32_e32 v123, 0x3fd9db23, v113
	v_mul_f32_e32 v124, 0xbfb8aa3b, v124
	v_mul_f32_e32 v125, 0xbfb8aa3b, v125
	v_mul_f32_e32 v123, 0xbfb8aa3b, v123
	v_exp_f32_e32 v124, v124
	v_exp_f32_e32 v125, v125
	v_exp_f32_e32 v123, v123
	v_add_f32_e32 v122, 1.0, v122
	v_add_f32_e32 v124, 1.0, v124
	v_add_f32_e32 v125, 1.0, v125
	v_add_f32_e32 v123, 1.0, v123
	v_add_f32_e32 v118, v118, v240
	v_rcp_f32_e32 v124, v124
	v_add_f32_e32 v119, v119, v241
	v_rcp_f32_e32 v125, v125
	v_add_f32_e32 v116, v116, v238
	v_rcp_f32_e32 v122, v122
	v_add_f32_e32 v117, v117, v239
	v_rcp_f32_e32 v123, v123
	v_med3_f32 v118, v118, s53, v194
	v_med3_f32 v119, v119, s53, v194
	v_med3_f32 v116, v116, s53, v194
	v_med3_f32 v117, v117, s53, v194
	v_pk_add_f32 v[118:119], v[118:119], 1.0 op_sel_hi:[1,0]
	v_pk_add_f32 v[116:117], v[116:117], 1.0 op_sel_hi:[1,0]
	v_pk_mul_f32 v[114:115], v[114:115], v[118:119]
	v_add_f32_e32 v108, v108, v252
	v_add_f32_e32 v109, v109, v253
	v_add_f32_e32 v110, v110, v254
	v_add_f32_e32 v111, v111, v255
	v_pk_mul_f32 v[112:113], v[112:113], v[116:117]
	v_pk_mul_f32 v[114:115], v[114:115], v[124:125]
	v_min_f32_e32 v108, 0x40e00000, v108
	v_min_f32_e32 v109, 0x40e00000, v109
	v_min_f32_e32 v110, 0x40e00000, v110
	v_min_f32_e32 v111, 0x40e00000, v111
	v_pk_mul_f32 v[112:113], v[112:113], v[122:123]
	v_cvt_pk_bf16_f32 v123, v114, v115
	v_mul_f32_e32 v114, 0x3fd9db23, v108
	v_mul_f32_e32 v115, 0x3fd9db23, v109
	v_mul_f32_e32 v116, 0x3fd9db23, v110
	v_mul_f32_e32 v117, 0x3fd9db23, v111
	v_mul_f32_e32 v114, 0xbfb8aa3b, v114
	v_mul_f32_e32 v115, 0xbfb8aa3b, v115
	v_mul_f32_e32 v116, 0xbfb8aa3b, v116
	v_mul_f32_e32 v117, 0xbfb8aa3b, v117
	v_exp_f32_e32 v114, v114
	v_exp_f32_e32 v115, v115
	v_exp_f32_e32 v116, v116
	v_exp_f32_e32 v117, v117
	v_add_f32_e32 v114, 1.0, v114
	v_add_f32_e32 v115, 1.0, v115
	v_add_f32_e32 v116, 1.0, v116
	v_add_f32_e32 v117, 1.0, v117
	v_add_f32_e32 v104, v104, v248
	v_rcp_f32_e32 v114, v114
	v_add_f32_e32 v105, v105, v249
	v_rcp_f32_e32 v115, v115
	v_add_f32_e32 v106, v106, v250
	v_rcp_f32_e32 v116, v116
	v_add_f32_e32 v107, v107, v251
	v_rcp_f32_e32 v117, v117
	v_med3_f32 v104, v104, s53, v194
	v_med3_f32 v105, v105, s53, v194
	v_med3_f32 v106, v106, s53, v194
	v_med3_f32 v107, v107, s53, v194
	v_pk_add_f32 v[104:105], v[104:105], 1.0 op_sel_hi:[1,0]
	v_pk_add_f32 v[106:107], v[106:107], 1.0 op_sel_hi:[1,0]
	v_pk_mul_f32 v[104:105], v[108:109], v[104:105]
	v_pk_mul_f32 v[106:107], v[110:111], v[106:107]
	v_add_f32_e32 v100, v100, v244
	v_pk_mul_f32 v[108:109], v[104:105], v[114:115]
	v_pk_mul_f32 v[104:105], v[106:107], v[116:117]
	v_min_f32_e32 v100, 0x40e00000, v100
	v_cvt_pk_bf16_f32 v105, v104, v105
	v_mul_f32_e32 v104, 0x3fd9db23, v100
	v_add_f32_e32 v102, v102, v246
	v_add_f32_e32 v103, v103, v247
	v_mul_f32_e32 v104, 0xbfb8aa3b, v104
	v_add_f32_e32 v101, v101, v245
	v_min_f32_e32 v102, 0x40e00000, v102
	v_min_f32_e32 v103, 0x40e00000, v103
	v_exp_f32_e32 v106, v104
	v_cvt_pk_bf16_f32 v104, v108, v109
	v_min_f32_e32 v101, 0x40e00000, v101
	v_mul_f32_e32 v108, 0x3fd9db23, v102
	v_mul_f32_e32 v109, 0x3fd9db23, v103
	v_mul_f32_e32 v107, 0x3fd9db23, v101
	v_mul_f32_e32 v108, 0xbfb8aa3b, v108
	v_mul_f32_e32 v109, 0xbfb8aa3b, v109
	v_mul_f32_e32 v107, 0xbfb8aa3b, v107
	v_exp_f32_e32 v108, v108
	v_exp_f32_e32 v109, v109
	v_exp_f32_e32 v107, v107
	v_add_f32_e32 v106, 1.0, v106
	v_add_f32_e32 v108, 1.0, v108
	v_add_f32_e32 v109, 1.0, v109
	v_add_f32_e32 v107, 1.0, v107
	v_add_f32_e32 v98, v98, v240
	v_rcp_f32_e32 v108, v108
	v_add_f32_e32 v99, v99, v241
	v_rcp_f32_e32 v109, v109
	v_add_f32_e32 v96, v96, v238
	v_rcp_f32_e32 v106, v106
	v_add_f32_e32 v97, v97, v239
	v_rcp_f32_e32 v107, v107
	v_med3_f32 v98, v98, s53, v194
	v_med3_f32 v99, v99, s53, v194
	v_med3_f32 v96, v96, s53, v194
	v_med3_f32 v97, v97, s53, v194
	v_pk_add_f32 v[98:99], v[98:99], 1.0 op_sel_hi:[1,0]
	v_pk_add_f32 v[96:97], v[96:97], 1.0 op_sel_hi:[1,0]
	v_pk_mul_f32 v[98:99], v[102:103], v[98:99]
	v_add_f32_e32 v92, v92, v252
	v_add_f32_e32 v93, v93, v253
	v_add_f32_e32 v94, v94, v254
	v_add_f32_e32 v95, v95, v255
	v_pk_mul_f32 v[96:97], v[100:101], v[96:97]
	v_pk_mul_f32 v[98:99], v[98:99], v[108:109]
	v_min_f32_e32 v92, 0x40e00000, v92
	v_min_f32_e32 v93, 0x40e00000, v93
	v_min_f32_e32 v94, 0x40e00000, v94
	v_min_f32_e32 v95, 0x40e00000, v95
	v_pk_mul_f32 v[96:97], v[96:97], v[106:107]
	v_cvt_pk_bf16_f32 v107, v98, v99
	v_mul_f32_e32 v98, 0x3fd9db23, v92
	v_mul_f32_e32 v99, 0x3fd9db23, v93
	v_mul_f32_e32 v100, 0x3fd9db23, v94
	v_mul_f32_e32 v101, 0x3fd9db23, v95
	v_mul_f32_e32 v98, 0xbfb8aa3b, v98
	v_mul_f32_e32 v99, 0xbfb8aa3b, v99
	v_mul_f32_e32 v100, 0xbfb8aa3b, v100
	v_mul_f32_e32 v101, 0xbfb8aa3b, v101
	v_exp_f32_e32 v98, v98
	v_exp_f32_e32 v99, v99
	v_exp_f32_e32 v100, v100
	v_exp_f32_e32 v101, v101
	v_add_f32_e32 v98, 1.0, v98
	v_add_f32_e32 v99, 1.0, v99
	v_add_f32_e32 v100, 1.0, v100
	v_add_f32_e32 v101, 1.0, v101
	v_add_f32_e32 v88, v88, v248
	v_rcp_f32_e32 v98, v98
	v_add_f32_e32 v89, v89, v249
	v_rcp_f32_e32 v99, v99
	v_add_f32_e32 v90, v90, v250
	v_rcp_f32_e32 v100, v100
	v_add_f32_e32 v91, v91, v251
	v_rcp_f32_e32 v101, v101
	v_med3_f32 v88, v88, s53, v194
	v_med3_f32 v89, v89, s53, v194
	v_med3_f32 v90, v90, s53, v194
	v_med3_f32 v91, v91, s53, v194
	v_pk_add_f32 v[88:89], v[88:89], 1.0 op_sel_hi:[1,0]
	v_pk_add_f32 v[90:91], v[90:91], 1.0 op_sel_hi:[1,0]
	v_pk_mul_f32 v[88:89], v[92:93], v[88:89]
	v_pk_mul_f32 v[90:91], v[94:95], v[90:91]
	v_add_f32_e32 v80, v80, v244
	v_pk_mul_f32 v[92:93], v[88:89], v[98:99]
	v_pk_mul_f32 v[88:89], v[90:91], v[100:101]
	v_min_f32_e32 v80, 0x40e00000, v80
	v_cvt_pk_bf16_f32 v89, v88, v89
	v_mul_f32_e32 v88, 0x3fd9db23, v80
	v_add_f32_e32 v82, v82, v246
	v_add_f32_e32 v83, v83, v247
	v_mul_f32_e32 v88, 0xbfb8aa3b, v88
	v_add_f32_e32 v81, v81, v245
	v_min_f32_e32 v82, 0x40e00000, v82
	v_min_f32_e32 v83, 0x40e00000, v83
	v_exp_f32_e32 v90, v88
	v_cvt_pk_bf16_f32 v88, v92, v93
	v_min_f32_e32 v81, 0x40e00000, v81
	v_mul_f32_e32 v92, 0x3fd9db23, v82
	v_mul_f32_e32 v93, 0x3fd9db23, v83
	v_mul_f32_e32 v91, 0x3fd9db23, v81
	v_mul_f32_e32 v92, 0xbfb8aa3b, v92
	v_mul_f32_e32 v93, 0xbfb8aa3b, v93
	v_mul_f32_e32 v91, 0xbfb8aa3b, v91
	v_exp_f32_e32 v92, v92
	v_exp_f32_e32 v93, v93
	v_exp_f32_e32 v91, v91
	v_add3_u32 v180, s68, 16, v178
	v_ashrrev_i32_e32 v181, 31, v180
	v_lshlrev_b64 v[180:181], 12, v[180:181]
	v_add_f32_e32 v92, 1.0, v92
	v_add_f32_e32 v93, 1.0, v93
	v_lshl_add_u64 v[180:181], s[50:51], 0, v[180:181]
	v_add_f32_e32 v90, 1.0, v90
	v_add_f32_e32 v91, 1.0, v91
	v_add_f32_e32 v86, v86, v240
	v_rcp_f32_e32 v92, v92
	v_add_f32_e32 v87, v87, v241
	v_rcp_f32_e32 v93, v93
	v_cvt_pk_bf16_f32 v170, v160, v161
	v_lshl_add_u64 v[160:161], v[180:181], 0, v[176:177]
	v_add_f32_e32 v84, v84, v238
	v_rcp_f32_e32 v90, v90
	v_add_f32_e32 v85, v85, v239
	v_rcp_f32_e32 v91, v91
	v_med3_f32 v86, v86, s53, v194
	v_med3_f32 v87, v87, s53, v194
	global_store_dwordx4 v[160:161], v[168:171], off
	v_add3_u32 v160, s68, 32, v178
	v_med3_f32 v84, v84, s53, v194
	v_med3_f32 v85, v85, s53, v194
	v_pk_add_f32 v[86:87], v[86:87], 1.0 op_sel_hi:[1,0]
	v_ashrrev_i32_e32 v161, 31, v160
	v_pk_add_f32 v[84:85], v[84:85], 1.0 op_sel_hi:[1,0]
	v_pk_mul_f32 v[82:83], v[82:83], v[86:87]
	v_add_f32_e32 v76, v76, v252
	v_add_f32_e32 v77, v77, v253
	v_add_f32_e32 v78, v78, v254
	v_add_f32_e32 v79, v79, v255
	v_lshlrev_b64 v[160:161], 12, v[160:161]
	v_pk_mul_f32 v[80:81], v[80:81], v[84:85]
	v_pk_mul_f32 v[82:83], v[82:83], v[92:93]
	v_min_f32_e32 v76, 0x40e00000, v76
	v_min_f32_e32 v77, 0x40e00000, v77
	v_min_f32_e32 v78, 0x40e00000, v78
	v_min_f32_e32 v79, 0x40e00000, v79
	v_add_f32_e32 v52, v52, v252
	v_add_f32_e32 v36, v36, v244
	v_lshl_add_u64 v[160:161], s[50:51], 0, v[160:161]
	v_pk_mul_f32 v[80:81], v[80:81], v[90:91]
	v_cvt_pk_bf16_f32 v91, v82, v83
	v_mul_f32_e32 v82, 0x3fd9db23, v76
	v_mul_f32_e32 v83, 0x3fd9db23, v77
	v_mul_f32_e32 v84, 0x3fd9db23, v78
	v_mul_f32_e32 v85, 0x3fd9db23, v79
	v_min_f32_e32 v52, 0x40e00000, v52
	v_min_f32_e32 v36, 0x40e00000, v36
	v_cvt_pk_bf16_f32 v154, v144, v145
	v_lshl_add_u64 v[144:145], v[160:161], 0, v[176:177]
	v_mul_f32_e32 v82, 0xbfb8aa3b, v82
	v_mul_f32_e32 v83, 0xbfb8aa3b, v83
	v_mul_f32_e32 v84, 0xbfb8aa3b, v84
	v_mul_f32_e32 v85, 0xbfb8aa3b, v85
	v_add_f32_e32 v68, v68, v244
	v_mul_f32_e32 v60, 0x3fd9db23, v52
	v_mul_f32_e32 v44, 0x3fd9db23, v36
	global_store_dwordx4 v[144:145], v[152:155], off
	v_add3_u32 v144, s68, 48, v178
	v_exp_f32_e32 v82, v82
	v_exp_f32_e32 v83, v83
	v_exp_f32_e32 v84, v84
	v_exp_f32_e32 v85, v85
	v_mul_f32_e32 v60, 0xbfb8aa3b, v60
	v_mul_f32_e32 v44, 0xbfb8aa3b, v44
	v_ashrrev_i32_e32 v145, 31, v144
	v_exp_f32_e32 v60, v60
	v_exp_f32_e32 v44, v44
	v_lshlrev_b64 v[144:145], 12, v[144:145]
	v_lshl_add_u64 v[144:145], s[50:51], 0, v[144:145]
	v_add_f32_e32 v53, v53, v253
	v_add_f32_e32 v37, v37, v245
	v_cvt_pk_bf16_f32 v138, v128, v129
	v_lshl_add_u64 v[128:129], v[144:145], 0, v[176:177]
	v_add_f32_e32 v82, 1.0, v82
	v_add_f32_e32 v83, 1.0, v83
	v_add_f32_e32 v84, 1.0, v84
	v_add_f32_e32 v85, 1.0, v85
	v_min_f32_e32 v53, 0x40e00000, v53
	v_min_f32_e32 v37, 0x40e00000, v37
	global_store_dwordx4 v[128:129], v[136:139], off
	v_add3_u32 v128, s68, 64, v178
	v_add_f32_e32 v72, v72, v248
	v_rcp_f32_e32 v82, v82
	v_add_f32_e32 v73, v73, v249
	v_rcp_f32_e32 v83, v83
	v_add_f32_e32 v74, v74, v250
	v_rcp_f32_e32 v84, v84
	v_add_f32_e32 v75, v75, v251
	v_rcp_f32_e32 v85, v85
	v_add_f32_e32 v64, v64, v238
	v_add_f32_e32 v48, v48, v248
	v_add_f32_e32 v56, 1.0, v60
	v_mul_f32_e32 v60, 0x3fd9db23, v53
	v_add_f32_e32 v32, v32, v238
	v_add_f32_e32 v40, 1.0, v44
	v_mul_f32_e32 v44, 0x3fd9db23, v37
	v_ashrrev_i32_e32 v129, 31, v128
	v_med3_f32 v72, v72, s53, v194
	v_med3_f32 v73, v73, s53, v194
	v_med3_f32 v74, v74, s53, v194
	v_med3_f32 v75, v75, s53, v194
	v_mul_f32_e32 v60, 0xbfb8aa3b, v60
	v_mul_f32_e32 v44, 0xbfb8aa3b, v44
	v_lshlrev_b64 v[128:129], 12, v[128:129]
	v_pk_add_f32 v[72:73], v[72:73], 1.0 op_sel_hi:[1,0]
	v_pk_add_f32 v[74:75], v[74:75], 1.0 op_sel_hi:[1,0]
	v_exp_f32_e32 v60, v60
	v_exp_f32_e32 v44, v44
	v_lshl_add_u64 v[128:129], s[50:51], 0, v[128:129]
	v_pk_mul_f32 v[74:75], v[78:79], v[74:75]
	v_pk_mul_f32 v[72:73], v[76:77], v[72:73]
	v_cvt_pk_bf16_f32 v122, v112, v113
	v_lshl_add_u64 v[112:113], v[128:129], 0, v[176:177]
	v_pk_mul_f32 v[76:77], v[72:73], v[82:83]
	v_pk_mul_f32 v[72:73], v[74:75], v[84:85]
	v_min_f32_e32 v68, 0x40e00000, v68
	v_add_f32_e32 v54, v54, v254
	v_add_f32_e32 v38, v38, v246
	global_store_dwordx4 v[112:113], v[120:123], off
	v_add_u32_e32 v112, s16, v178
	v_cvt_pk_bf16_f32 v73, v72, v73
	v_mul_f32_e32 v72, 0x3fd9db23, v68
	v_add_f32_e32 v69, v69, v245
	v_add_f32_e32 v70, v70, v246
	v_add_f32_e32 v71, v71, v247
	v_min_f32_e32 v54, 0x40e00000, v54
	v_min_f32_e32 v38, 0x40e00000, v38
	v_ashrrev_i32_e32 v113, 31, v112
	v_mul_f32_e32 v72, 0xbfb8aa3b, v72
	v_min_f32_e32 v69, 0x40e00000, v69
	v_add_f32_e32 v65, v65, v239
	v_min_f32_e32 v70, 0x40e00000, v70
	v_min_f32_e32 v71, 0x40e00000, v71
	v_add_f32_e32 v49, v49, v249
	v_add_f32_e32 v57, 1.0, v60
	v_mul_f32_e32 v60, 0x3fd9db23, v54
	v_add_f32_e32 v33, v33, v239
	v_add_f32_e32 v41, 1.0, v44
	v_mul_f32_e32 v44, 0x3fd9db23, v38
	v_lshlrev_b64 v[112:113], 12, v[112:113]
	v_exp_f32_e32 v74, v72
	v_cvt_pk_bf16_f32 v72, v76, v77
	v_mul_f32_e32 v75, 0x3fd9db23, v69
	v_mul_f32_e32 v76, 0x3fd9db23, v70
	v_mul_f32_e32 v77, 0x3fd9db23, v71
	v_mul_f32_e32 v60, 0xbfb8aa3b, v60
	v_mul_f32_e32 v44, 0xbfb8aa3b, v44
	v_lshl_add_u64 v[112:113], s[50:51], 0, v[112:113]
	v_mul_f32_e32 v75, 0xbfb8aa3b, v75
	v_mul_f32_e32 v76, 0xbfb8aa3b, v76
	v_mul_f32_e32 v77, 0xbfb8aa3b, v77
	v_exp_f32_e32 v60, v60
	v_exp_f32_e32 v44, v44
	v_cvt_pk_bf16_f32 v106, v96, v97
	v_lshl_add_u64 v[96:97], v[112:113], 0, v[176:177]
	s_add_i32 s16, s68, 0x60
	v_exp_f32_e32 v75, v75
	v_exp_f32_e32 v76, v76
	v_exp_f32_e32 v77, v77
	global_store_dwordx4 v[96:97], v[104:107], off
	v_add_u32_e32 v96, s16, v178
	v_add_f32_e32 v55, v55, v255
	v_add_f32_e32 v39, v39, v247
	v_ashrrev_i32_e32 v97, 31, v96
	v_min_f32_e32 v55, 0x40e00000, v55
	v_min_f32_e32 v39, 0x40e00000, v39
	v_lshlrev_b64 v[96:97], 12, v[96:97]
	v_add_f32_e32 v66, v66, v240
	v_add_f32_e32 v50, v50, v250
	v_add_f32_e32 v58, 1.0, v60
	v_mul_f32_e32 v60, 0x3fd9db23, v55
	v_add_f32_e32 v34, v34, v240
	v_add_f32_e32 v42, 1.0, v44
	v_mul_f32_e32 v44, 0x3fd9db23, v39
	v_lshl_add_u64 v[96:97], s[50:51], 0, v[96:97]
	v_add_f32_e32 v74, 1.0, v74
	v_add_f32_e32 v75, 1.0, v75
	v_add_f32_e32 v76, 1.0, v76
	v_add_f32_e32 v77, 1.0, v77
	v_mul_f32_e32 v60, 0xbfb8aa3b, v60
	v_mul_f32_e32 v44, 0xbfb8aa3b, v44
	v_cvt_pk_bf16_f32 v90, v80, v81
	v_lshl_add_u64 v[80:81], v[96:97], 0, v[176:177]
	s_add_i32 s16, s68, 0x70
	v_rcp_f32_e32 v74, v74
	v_rcp_f32_e32 v75, v75
	v_rcp_f32_e32 v76, v76
	v_add_f32_e32 v67, v67, v241
	v_rcp_f32_e32 v77, v77
	v_exp_f32_e32 v60, v60
	v_exp_f32_e32 v44, v44
	global_store_dwordx4 v[80:81], v[88:91], off
	v_add_u32_e32 v80, s16, v178
	v_med3_f32 v64, v64, s53, v194
	v_med3_f32 v65, v65, s53, v194
	v_med3_f32 v66, v66, s53, v194
	v_med3_f32 v67, v67, s53, v194
	v_ashrrev_i32_e32 v81, 31, v80
	v_pk_add_f32 v[64:65], v[64:65], 1.0 op_sel_hi:[1,0]
	v_pk_add_f32 v[66:67], v[66:67], 1.0 op_sel_hi:[1,0]
	v_lshlrev_b64 v[80:81], 12, v[80:81]
	v_pk_mul_f32 v[66:67], v[70:71], v[66:67]
	v_pk_mul_f32 v[64:65], v[68:69], v[64:65]
	v_lshl_add_u64 v[80:81], s[50:51], 0, v[80:81]
	v_pk_mul_f32 v[64:65], v[64:65], v[74:75]
	v_pk_mul_f32 v[66:67], v[66:67], v[76:77]
	v_add_f32_e32 v51, v51, v251
	v_add_f32_e32 v59, 1.0, v60
	v_add_f32_e32 v35, v35, v241
	v_add_f32_e32 v43, 1.0, v44
	v_cvt_pk_bf16_f32 v75, v66, v67
	v_cvt_pk_bf16_f32 v74, v64, v65
	v_lshl_add_u64 v[64:65], v[80:81], 0, v[176:177]
	s_add_i32 s16, s68, 0x80
	v_rcp_f32_e32 v56, v56
	v_rcp_f32_e32 v57, v57
	v_rcp_f32_e32 v58, v58
	v_rcp_f32_e32 v59, v59
	v_rcp_f32_e32 v40, v40
	v_rcp_f32_e32 v41, v41
	v_rcp_f32_e32 v42, v42
	v_rcp_f32_e32 v43, v43
	global_store_dwordx4 v[64:65], v[72:75], off
	v_add_u32_e32 v64, s16, v178
	v_med3_f32 v48, v48, s53, v194
	v_med3_f32 v49, v49, s53, v194
	v_med3_f32 v50, v50, s53, v194
	v_med3_f32 v51, v51, s53, v194
	v_med3_f32 v32, v32, s53, v194
	v_med3_f32 v33, v33, s53, v194
	v_med3_f32 v34, v34, s53, v194
	v_med3_f32 v35, v35, s53, v194
	v_ashrrev_i32_e32 v65, 31, v64
	v_pk_add_f32 v[48:49], v[48:49], 1.0 op_sel_hi:[1,0]
	v_pk_add_f32 v[50:51], v[50:51], 1.0 op_sel_hi:[1,0]
	v_pk_add_f32 v[32:33], v[32:33], 1.0 op_sel_hi:[1,0]
	v_pk_add_f32 v[34:35], v[34:35], 1.0 op_sel_hi:[1,0]
	v_lshlrev_b64 v[64:65], 12, v[64:65]
	v_pk_mul_f32 v[50:51], v[54:55], v[50:51]
	v_pk_mul_f32 v[48:49], v[52:53], v[48:49]
	v_pk_mul_f32 v[34:35], v[38:39], v[34:35]
	v_pk_mul_f32 v[32:33], v[36:37], v[32:33]
	v_lshl_add_u64 v[64:65], s[50:51], 0, v[64:65]
	v_pk_mul_f32 v[52:53], v[48:49], v[56:57]
	v_pk_mul_f32 v[48:49], v[50:51], v[58:59]
	v_pk_mul_f32 v[32:33], v[32:33], v[40:41]
	v_pk_mul_f32 v[34:35], v[34:35], v[42:43]
	v_cvt_pk_bf16_f32 v49, v48, v49
	v_cvt_pk_bf16_f32 v48, v52, v53
	v_cvt_pk_bf16_f32 v51, v34, v35
	v_cvt_pk_bf16_f32 v50, v32, v33
	v_lshl_add_u64 v[32:33], v[64:65], 0, v[176:177]
	s_mov_b32 s68, s43
	global_store_dwordx4 v[32:33], v[48:51], off
	s_cbranch_vccnz .LBB0_663
